# lru unit: carry across the four segments read together and applied under scalar compares instead of three exec-masked blocks
# baseline (speedup 1.0000x reference)
.LBB0_370:
	v_ashrrev_i32_e32 v11, 6, v30
	v_add_u32_e32 v8, v111, v104
	s_waitcnt lgkmcnt(0)
	s_barrier
	v_lshl_add_u32 v22, v11, 8, v8
	ds_read2st64_b32 v[112:113], v22 offset1:1
	ds_read2st64_b32 v[114:115], v22 offset0:2 offset1:3
	ds_read2st64_b32 v[116:117], v22 offset0:8 offset1:9
	ds_read2st64_b32 v[118:119], v22 offset0:10 offset1:11
	ds_read2st64_b32 v[120:121], v22 offset0:16 offset1:17
	ds_read2st64_b32 v[122:123], v22 offset0:18 offset1:19
	ds_read2st64_b32 v[124:125], v22 offset0:24 offset1:25
	ds_read2st64_b32 v[126:127], v22 offset0:26 offset1:27
	ds_read2st64_b32 v[128:129], v22 offset0:32 offset1:33
	ds_read2st64_b32 v[130:131], v22 offset0:34 offset1:35
	ds_read2st64_b32 v[132:133], v22 offset0:40 offset1:41
	ds_read2st64_b32 v[134:135], v22 offset0:42 offset1:43
	ds_read2st64_b32 v[136:137], v22 offset0:48 offset1:49
	ds_read2st64_b32 v[138:139], v22 offset0:50 offset1:51
	ds_read2st64_b32 v[140:141], v22 offset0:56 offset1:57
	ds_read2st64_b32 v[142:143], v22 offset0:58 offset1:59
	v_lshlrev_b32_e32 v9, 1, v31
	s_movk_i32 s0, 0x104
	v_sub_u32_e32 v10, v8, v9
	v_mad_u64_u32 v[8:9], s[0:1], v11, s0, v[8:9]
	s_waitcnt vmcnt(12) lgkmcnt(0)
	v_fma_f32 v23, v15, v112, v14
	v_fmac_f32_e32 v23, v21, v113
	v_mad_u64_u32 v[10:11], s[0:1], v11, s39, v[10:11]
	s_or_b32 s0, s24, s71
	s_ashr_i32 s1, s0, 31
	v_fmac_f32_e32 v23, v12, v114
	v_fmac_f32_e32 v23, v13, v115
	ds_write_b32 v8, v23 offset:17408
	v_bfe_u32 v9, v23, 16, 1
	v_add3_u32 v9, v23, v9, s25
	ds_write_b16_d16_hi v10, v9 offset:34304
	s_lshl_b64 s[0:1], s[0:1], 13
	v_fma_f32 v9, v15, v116, v14
	v_fmac_f32_e32 v9, v21, v117
	s_add_u32 s2, s69, s0
	s_addc_u32 s3, s70, s1
	v_and_b32_e32 v24, 48, v30
	v_mov_b32_e32 v25, v105
	v_fmac_f32_e32 v9, v12, v118
	v_fmac_f32_e32 v9, v13, v119
	ds_write_b32 v8, v9 offset:19488
	v_bfe_u32 v11, v9, 16, 1
	v_add3_u32 v9, v9, v11, s25
	ds_write_b16_d16_hi v10, v9 offset:35456
	s_or_b32 s0, s24, s72
	v_fma_f32 v9, v15, v120, v14
	v_fmac_f32_e32 v9, v21, v121
	s_ashr_i32 s1, s0, 31
	s_lshl_b64 s[0:1], s[0:1], 13
	s_add_u32 s0, s69, s0
	s_addc_u32 s1, s70, s1
	v_fmac_f32_e32 v9, v12, v122
	v_fmac_f32_e32 v9, v13, v123
	ds_write_b32 v8, v9 offset:21568
	v_bfe_u32 v11, v9, 16, 1
	v_add3_u32 v9, v9, v11, s25
	ds_write_b16_d16_hi v10, v9 offset:36608
	s_mov_b32 s14, 0xbfb8aa3b
	v_fma_f32 v9, v15, v124, v14
	v_fmac_f32_e32 v9, v21, v125
	v_or_b32_e32 v47, 16, v35
	v_cmp_gt_u32_e32 vcc, s21, v30
	v_mov_b32_e32 v67, 1.0
	v_mov_b32_e32 v68, 0
	v_fmac_f32_e32 v9, v12, v126
	v_fmac_f32_e32 v9, v13, v127
	ds_write_b32 v8, v9 offset:23648
	v_bfe_u32 v11, v9, 16, 1
	v_add3_u32 v9, v9, v11, s25
	ds_write_b16_d16_hi v10, v9 offset:37760
	v_fma_f32 v9, v15, v128, v14
	v_fmac_f32_e32 v9, v21, v129
	v_fmac_f32_e32 v9, v12, v130
	v_fmac_f32_e32 v9, v13, v131
	ds_write_b32 v8, v9 offset:25728
	v_bfe_u32 v11, v9, 16, 1
	v_add3_u32 v9, v9, v11, s25
	ds_write_b16_d16_hi v10, v9 offset:38912
	v_fma_f32 v9, v15, v132, v14
	v_fmac_f32_e32 v9, v21, v133
	v_fmac_f32_e32 v9, v12, v134
	v_fmac_f32_e32 v9, v13, v135
	ds_write_b32 v8, v9 offset:27808
	v_bfe_u32 v11, v9, 16, 1
	v_add3_u32 v9, v9, v11, s25
	ds_write_b16_d16_hi v10, v9 offset:40064
	v_fma_f32 v9, v15, v136, v14
	v_fmac_f32_e32 v9, v21, v137
	v_fmac_f32_e32 v9, v12, v138
	v_fmac_f32_e32 v9, v13, v139
	ds_write_b32 v8, v9 offset:29888
	v_bfe_u32 v11, v9, 16, 1
	v_add3_u32 v9, v9, v11, s25
	ds_write_b16_d16_hi v10, v9 offset:41216
	v_fmac_f32_e32 v14, v15, v140
	v_fmac_f32_e32 v14, v21, v141
	v_fmac_f32_e32 v14, v12, v142
	v_fmac_f32_e32 v14, v13, v143
	ds_write_b32 v8, v14 offset:31968
	v_bfe_u32 v8, v14, 16, 1
	v_add3_u32 v8, v14, v8, s25
	v_lshrrev_b32_e32 v16, 2, v30
	ds_write_b16_d16_hi v10, v8 offset:42368
	v_or_b32_e32 v8, s34, v35
	v_and_or_b32 v21, v16, 12, s34
	v_lshlrev_b32_e32 v16, 7, v35
	v_mov_b32_e32 v17, v105
	v_mul_u32_u24_e32 v8, 0x90, v8
	v_lshl_add_u64 v[22:23], s[2:3], 0, v[16:17]
	s_waitcnt lgkmcnt(0)
	s_barrier
	v_add3_u32 v8, v111, v8, v24
	v_lshl_add_u64 v[22:23], v[22:23], 0, v[24:25]
	ds_read_b128 v[12:15], v8 offset:34304
	ds_read_b128 v[8:11], v8 offset:34368
	global_load_dwordx4 v[36:39], v[22:23], off
	global_load_dwordx4 v[48:51], v[22:23], off offset:64
	v_lshl_add_u64 v[16:17], s[0:1], 0, v[16:17]
	v_lshl_add_u64 v[16:17], v[16:17], 0, v[24:25]
	v_lshlrev_b32_e32 v42, 6, v21
	s_waitcnt vmcnt(1) lgkmcnt(1)
	v_mfma_f32_16x16x32_bf16 v[36:39], v[12:15], v[36:39], 0
	global_load_dwordx4 v[52:55], v[16:17], off offset:64
	s_waitcnt vmcnt(1) lgkmcnt(0)
	v_mfma_f32_16x16x32_bf16 v[48:51], v[8:11], v[48:51], v[36:39]
	s_nop 4
	global_load_dwordx4 v[36:39], v[16:17], off
	v_mul_f32_e64 v17, |v20|, s14
	s_nop 0
	v_add_f32_e32 v22, v18, v48
	v_mul_f32_e32 v22, 0xbfb8aa3b, v22
	v_exp_f32_e32 v17, v17
	v_exp_f32_e32 v22, v22
	v_max_f32_e64 v16, -v20, -v20
	v_max_f32_e32 v16, 0, v16
	v_add_f32_e32 v17, 1.0, v17
	v_add_f32_e32 v22, 1.0, v22
	v_log_f32_e32 v17, v17
	v_rcp_f32_e32 v22, v22
	v_or_b32_e32 v20, s73, v35
	v_lshlrev_b32_e32 v48, 7, v47
	v_fmac_f32_e32 v16, 0x3f317218, v17
	v_mul_f32_e32 v22, 0xc1000000, v22
	v_mul_f32_e32 v22, v16, v22
	v_mul_f32_e32 v22, 0x3fb8aa3b, v22
	v_exp_f32_e32 v22, v22
	v_lshlrev_b32_e32 v17, 2, v35
	s_waitcnt vmcnt(0)
	v_mfma_f32_16x16x32_bf16 v[36:39], v[12:15], v[36:39], 0
	v_mfma_f32_16x16x32_bf16 v[52:55], v[8:11], v[52:55], v[36:39]
	s_nop 6
	v_fma_f32 v36, -v22, v22, 1.0
	v_max_f32_e32 v36, 0, v36
	v_add_f32_e32 v23, v19, v52
	v_mul_f32_e32 v23, 0xbfb8aa3b, v23
	v_exp_f32_e32 v23, v23
	v_sqrt_f32_e32 v36, v36
	v_or_b32_e32 v39, 64, v42
	v_or_b32_e32 v38, 0x80, v42
	v_add_f32_e32 v23, 1.0, v23
	v_rcp_f32_e32 v23, v23
	v_or_b32_e32 v37, 0xc0, v42
	v_mul_f32_e32 v23, v23, v36
	v_mul_u32_u24_e32 v36, 0x104, v21
	v_add3_u32 v36, v111, v17, v36
	ds_read_b32 v144, v36 offset:17408
	ds_read_b32 v145, v36 offset:17668
	ds_read_b32 v146, v36 offset:17928
	ds_read_b32 v147, v36 offset:18188
	ds_read_b32 v148, v36 offset:17472
	ds_read_b32 v149, v36 offset:17732
	ds_read_b32 v150, v36 offset:17992
	ds_read_b32 v151, v36 offset:18252
	ds_read_b32 v152, v36 offset:17536
	ds_read_b32 v153, v36 offset:17796
	ds_read_b32 v154, v36 offset:18056
	ds_read_b32 v155, v36 offset:18316
	ds_read_b32 v156, v36 offset:17600
	ds_read_b32 v157, v36 offset:17860
	ds_read_b32 v158, v36 offset:18120
	ds_read_b32 v159, v36 offset:18380
	v_or_b32_e32 v21, v42, v20
	v_lshlrev_b32_e32 v21, 2, v21
	s_waitcnt lgkmcnt(0)
	v_mul_f32_e32 v17, v144, v23
	v_add_u32_e32 v23, v111, v21
	v_add_u32_e32 v21, v28, v21
	ds_write_b32 v23, v22 offset:43520
	ds_write_b32 v21, v17
	v_add_f32_e32 v17, v18, v49
	v_mul_f32_e32 v17, 0xbfb8aa3b, v17
	v_exp_f32_e32 v17, v17
	v_add_f32_e32 v21, v19, v53
	v_mul_f32_e32 v21, 0xbfb8aa3b, v21
	v_exp_f32_e32 v21, v21
	v_add_f32_e32 v17, 1.0, v17
	v_rcp_f32_e32 v17, v17
	v_mov_b32_e32 v49, v105
	v_add_f32_e32 v21, 1.0, v21
	v_rcp_f32_e32 v21, v21
	v_mul_f32_e32 v17, 0xc1000000, v17
	v_mul_f32_e32 v17, v16, v17
	v_mul_f32_e32 v17, 0x3fb8aa3b, v17
	v_exp_f32_e32 v17, v17
	s_nop 0
	v_fma_f32 v22, -v17, v17, 1.0
	v_max_f32_e32 v22, 0, v22
	v_sqrt_f32_e32 v22, v22
	s_nop 0
	v_mul_f32_e32 v21, v21, v22
	v_mul_f32_e32 v21, v145, v21
	v_or_b32_e32 v22, v39, v20
	v_lshlrev_b32_e32 v22, 2, v22
	v_add_u32_e32 v23, v111, v22
	ds_write_b32 v23, v17 offset:43520
	v_add_u32_e32 v17, v28, v22
	ds_write_b32 v17, v21
	v_add_f32_e32 v17, v18, v50
	v_mul_f32_e32 v17, 0xbfb8aa3b, v17
	v_exp_f32_e32 v17, v17
	v_add_f32_e32 v21, v19, v54
	v_mul_f32_e32 v21, 0xbfb8aa3b, v21
	v_exp_f32_e32 v21, v21
	v_add_f32_e32 v17, 1.0, v17
	v_rcp_f32_e32 v17, v17
	v_add_f32_e32 v21, 1.0, v21
	v_rcp_f32_e32 v21, v21
	v_mul_f32_e32 v17, 0xc1000000, v17
	v_mul_f32_e32 v17, v16, v17
	v_mul_f32_e32 v17, 0x3fb8aa3b, v17
	v_exp_f32_e32 v17, v17
	s_nop 0
	v_fma_f32 v22, -v17, v17, 1.0
	v_max_f32_e32 v22, 0, v22
	v_sqrt_f32_e32 v22, v22
	s_nop 0
	v_mul_f32_e32 v21, v21, v22
	v_mul_f32_e32 v21, v146, v21
	v_or_b32_e32 v22, v38, v20
	v_lshlrev_b32_e32 v22, 2, v22
	v_add_u32_e32 v23, v111, v22
	ds_write_b32 v23, v17 offset:43520
	v_add_u32_e32 v17, v28, v22
	ds_write_b32 v17, v21
	v_add_f32_e32 v17, v18, v51
	v_mul_f32_e32 v17, 0xbfb8aa3b, v17
	v_exp_f32_e32 v17, v17
	v_add_f32_e32 v18, v19, v55
	v_mul_f32_e32 v18, 0xbfb8aa3b, v18
	v_exp_f32_e32 v18, v18
	v_add_f32_e32 v17, 1.0, v17
	v_rcp_f32_e32 v17, v17
	v_add_f32_e32 v18, 1.0, v18
	v_rcp_f32_e32 v18, v18
	v_mul_f32_e32 v17, 0xc1000000, v17
	v_mul_f32_e32 v16, v16, v17
	v_mul_f32_e32 v16, 0x3fb8aa3b, v16
	v_exp_f32_e32 v16, v16
	s_nop 0
	v_fma_f32 v17, -v16, v16, 1.0
	v_max_f32_e32 v17, 0, v17
	v_sqrt_f32_e32 v17, v17
	s_nop 0
	v_mul_f32_e32 v17, v18, v17
	v_mul_f32_e32 v17, v147, v17
	v_or_b32_e32 v18, v37, v20
	v_lshlrev_b32_e32 v18, 2, v18
	v_add_u32_e32 v19, v111, v18
	ds_write_b32 v19, v16 offset:43520
	v_add_u32_e32 v16, v28, v18
	ds_write_b32 v16, v17
	v_lshl_add_u64 v[16:17], s[2:3], 0, v[48:49]
	v_lshl_add_u64 v[20:21], v[16:17], 0, v[24:25]
	global_load_dwordx4 v[16:19], v[20:21], off
	s_waitcnt vmcnt(0)
	v_mfma_f32_16x16x32_bf16 v[16:19], v[12:15], v[16:19], 0
	global_load_dwordx4 v[20:23], v[20:21], off offset:64
	s_waitcnt vmcnt(0)
	v_mfma_f32_16x16x32_bf16 v[16:19], v[8:11], v[20:23], v[16:19]
	v_lshl_add_u64 v[20:21], s[0:1], 0, v[48:49]
	v_lshl_add_u64 v[48:49], v[20:21], 0, v[24:25]
	global_load_dwordx4 v[20:23], v[48:49], off
	s_waitcnt vmcnt(0)
	v_mfma_f32_16x16x32_bf16 v[20:23], v[12:15], v[20:23], 0
	global_load_dwordx4 v[48:51], v[48:49], off offset:64
	s_nop 1
	v_add_f32_e32 v16, v45, v16
	v_mul_f32_e32 v16, 0xbfb8aa3b, v16
	s_waitcnt vmcnt(0)
	v_mfma_f32_16x16x32_bf16 v[20:23], v[8:11], v[48:51], v[20:23]
	v_max_f32_e64 v48, -v46, -v46
	v_mul_f32_e64 v46, |v46|, s14
	v_exp_f32_e32 v46, v46
	v_exp_f32_e32 v16, v16
	v_max_f32_e32 v49, 0, v48
	s_nop 2
	v_add_f32_e32 v20, v44, v20
	v_add_f32_e32 v46, 1.0, v46
	v_add_f32_e32 v16, 1.0, v16
	v_log_f32_e32 v46, v46
	v_rcp_f32_e32 v16, v16
	v_mul_f32_e32 v20, 0xbfb8aa3b, v20
	v_exp_f32_e32 v20, v20
	v_fmac_f32_e32 v49, 0x3f317218, v46
	v_mul_f32_e32 v16, 0xc1000000, v16
	v_mul_f32_e32 v16, v49, v16
	v_mul_f32_e32 v16, 0x3fb8aa3b, v16
	v_exp_f32_e32 v16, v16
	v_add_f32_e32 v20, 1.0, v20
	v_rcp_f32_e32 v20, v20
	v_add_u32_e32 v51, s73, v35
	v_fma_f32 v46, -v16, v16, 1.0
	v_max_f32_e32 v46, 0, v46
	v_sqrt_f32_e32 v46, v46
	v_or_b32_e32 v50, s73, v47
	v_add_u32_e32 v47, v42, v51
	v_lshl_add_u32 v48, v47, 2, v111
	v_mul_f32_e32 v20, v20, v46
	ds_write_b32 v48, v16 offset:43584
	v_mul_f32_e32 v20, v148, v20
	v_or_b32_e32 v46, v42, v50
	v_lshl_add_u32 v16, v46, 2, v28
	ds_write_b32 v16, v20
	v_add_f32_e32 v16, v45, v17
	v_mul_f32_e32 v16, 0xbfb8aa3b, v16
	v_exp_f32_e32 v16, v16
	v_add_f32_e32 v17, v44, v21
	v_mul_f32_e32 v17, 0xbfb8aa3b, v17
	v_exp_f32_e32 v17, v17
	v_add_f32_e32 v16, 1.0, v16
	v_rcp_f32_e32 v16, v16
	v_add_u32_e32 v21, v39, v51
	v_add_f32_e32 v17, 1.0, v17
	v_rcp_f32_e32 v17, v17
	v_mul_f32_e32 v16, 0xc1000000, v16
	v_mul_f32_e32 v16, v49, v16
	v_mul_f32_e32 v16, 0x3fb8aa3b, v16
	v_exp_f32_e32 v16, v16
	v_lshl_add_u32 v47, v21, 2, v111
	v_fma_f32 v20, -v16, v16, 1.0
	v_max_f32_e32 v20, 0, v20
	v_sqrt_f32_e32 v20, v20
	s_nop 0
	v_mul_f32_e32 v17, v17, v20
	ds_write_b32 v47, v16 offset:43584
	v_mul_f32_e32 v17, v149, v17
	v_or_b32_e32 v20, v39, v50
	v_lshl_add_u32 v16, v20, 2, v28
	ds_write_b32 v16, v17
	v_add_f32_e32 v16, v45, v18
	v_mul_f32_e32 v16, 0xbfb8aa3b, v16
	v_exp_f32_e32 v16, v16
	v_add_f32_e32 v17, v44, v22
	v_mul_f32_e32 v17, 0xbfb8aa3b, v17
	v_exp_f32_e32 v17, v17
	v_add_f32_e32 v16, 1.0, v16
	v_rcp_f32_e32 v16, v16
	v_add_u32_e32 v20, v38, v51
	v_add_f32_e32 v17, 1.0, v17
	v_rcp_f32_e32 v17, v17
	v_mul_f32_e32 v16, 0xc1000000, v16
	v_mul_f32_e32 v16, v49, v16
	v_mul_f32_e32 v16, 0x3fb8aa3b, v16
	v_exp_f32_e32 v16, v16
	v_lshl_add_u32 v46, v20, 2, v111
	v_fma_f32 v18, -v16, v16, 1.0
	v_max_f32_e32 v18, 0, v18
	v_sqrt_f32_e32 v18, v18
	s_nop 0
	v_mul_f32_e32 v17, v17, v18
	ds_write_b32 v46, v16 offset:43584
	v_mul_f32_e32 v17, v150, v17
	v_or_b32_e32 v18, v38, v50
	v_lshl_add_u32 v16, v18, 2, v28
	ds_write_b32 v16, v17
	v_add_f32_e32 v16, v45, v19
	v_mul_f32_e32 v16, 0xbfb8aa3b, v16
	v_exp_f32_e32 v16, v16
	v_add_f32_e32 v17, v44, v23
	v_mul_f32_e32 v17, 0xbfb8aa3b, v17
	v_exp_f32_e32 v17, v17
	v_add_f32_e32 v16, 1.0, v16
	v_rcp_f32_e32 v16, v16
	v_add_u32_e32 v19, v37, v51
	v_add_f32_e32 v17, 1.0, v17
	v_rcp_f32_e32 v17, v17
	v_mul_f32_e32 v16, 0xc1000000, v16
	v_mul_f32_e32 v16, v49, v16
	v_mul_f32_e32 v16, 0x3fb8aa3b, v16
	v_exp_f32_e32 v16, v16
	v_lshl_add_u32 v44, v19, 2, v111
	v_or_b32_e32 v45, 32, v35
	v_mov_b32_e32 v51, v105
	v_fma_f32 v18, -v16, v16, 1.0
	v_max_f32_e32 v18, 0, v18
	v_sqrt_f32_e32 v18, v18
	v_max_f32_e64 v49, -v43, -v43
	v_mul_f32_e64 v43, |v43|, s14
	v_exp_f32_e32 v43, v43
	v_mul_f32_e32 v17, v17, v18
	ds_write_b32 v44, v16 offset:43584
	v_add_f32_e32 v43, 1.0, v43
	v_log_f32_e32 v43, v43
	v_max_f32_e32 v49, 0, v49
	v_mul_f32_e32 v17, v151, v17
	v_or_b32_e32 v18, v37, v50
	v_lshl_add_u32 v16, v18, 2, v28
	v_lshlrev_b32_e32 v50, 7, v45
	ds_write_b32 v16, v17
	v_lshl_add_u64 v[16:17], s[2:3], 0, v[50:51]
	v_lshl_add_u64 v[20:21], v[16:17], 0, v[24:25]
	global_load_dwordx4 v[16:19], v[20:21], off
	s_waitcnt vmcnt(0)
	v_mfma_f32_16x16x32_bf16 v[16:19], v[12:15], v[16:19], 0
	global_load_dwordx4 v[20:23], v[20:21], off offset:64
	v_fmac_f32_e32 v49, 0x3f317218, v43
	v_or_b32_e32 v43, s73, v45
	s_waitcnt vmcnt(0)
	v_mfma_f32_16x16x32_bf16 v[16:19], v[8:11], v[20:23], v[16:19]
	v_lshl_add_u64 v[20:21], s[0:1], 0, v[50:51]
	v_lshl_add_u64 v[50:51], v[20:21], 0, v[24:25]
	global_load_dwordx4 v[20:23], v[50:51], off
	s_nop 4
	v_add_f32_e32 v16, v41, v16
	global_load_dwordx4 v[50:53], v[50:51], off offset:64
	v_mul_f32_e32 v16, 0xbfb8aa3b, v16
	v_exp_f32_e32 v16, v16
	s_waitcnt vmcnt(1)
	v_mfma_f32_16x16x32_bf16 v[20:23], v[12:15], v[20:23], 0
	v_add_f32_e32 v16, 1.0, v16
	v_rcp_f32_e32 v16, v16
	v_or_b32_e32 v35, 48, v35
	s_waitcnt vmcnt(0)
	v_mfma_f32_16x16x32_bf16 v[20:23], v[8:11], v[50:53], v[20:23]
	v_mul_f32_e32 v16, 0xc1000000, v16
	v_mul_f32_e32 v16, v49, v16
	v_mul_f32_e32 v16, 0x3fb8aa3b, v16
	v_exp_f32_e32 v16, v16
	s_nop 3
	v_add_f32_e32 v20, v40, v20
	v_mul_f32_e32 v20, 0xbfb8aa3b, v20
	v_exp_f32_e32 v20, v20
	v_fma_f32 v45, -v16, v16, 1.0
	v_max_f32_e32 v45, 0, v45
	v_sqrt_f32_e32 v45, v45
	v_add_f32_e32 v20, 1.0, v20
	v_rcp_f32_e32 v20, v20
	s_nop 0
	v_mul_f32_e32 v20, v20, v45
	ds_write_b32 v48, v16 offset:43648
	v_mul_f32_e32 v20, v152, v20
	v_or_b32_e32 v45, v42, v43
	v_lshl_add_u32 v16, v45, 2, v28
	ds_write_b32 v16, v20
	v_add_f32_e32 v16, v41, v17
	v_mul_f32_e32 v16, 0xbfb8aa3b, v16
	v_exp_f32_e32 v16, v16
	v_add_f32_e32 v17, v40, v21
	v_mul_f32_e32 v17, 0xbfb8aa3b, v17
	v_exp_f32_e32 v17, v17
	v_add_f32_e32 v16, 1.0, v16
	v_rcp_f32_e32 v16, v16
	v_add_f32_e32 v17, 1.0, v17
	v_rcp_f32_e32 v17, v17
	v_mul_f32_e32 v16, 0xc1000000, v16
	v_mul_f32_e32 v16, v49, v16
	v_mul_f32_e32 v16, 0x3fb8aa3b, v16
	v_exp_f32_e32 v16, v16
	s_nop 0
	v_fma_f32 v20, -v16, v16, 1.0
	v_max_f32_e32 v20, 0, v20
	v_sqrt_f32_e32 v20, v20
	s_nop 0
	v_mul_f32_e32 v17, v17, v20
	ds_write_b32 v47, v16 offset:43648
	v_mul_f32_e32 v17, v153, v17
	v_or_b32_e32 v20, v39, v43
	v_lshl_add_u32 v16, v20, 2, v28
	ds_write_b32 v16, v17
	v_add_f32_e32 v16, v41, v18
	v_mul_f32_e32 v16, 0xbfb8aa3b, v16
	v_exp_f32_e32 v16, v16
	v_add_f32_e32 v17, v40, v22
	v_mul_f32_e32 v17, 0xbfb8aa3b, v17
	v_exp_f32_e32 v17, v17
	v_add_f32_e32 v16, 1.0, v16
	v_rcp_f32_e32 v16, v16
	v_add_f32_e32 v17, 1.0, v17
	v_rcp_f32_e32 v17, v17
	v_mul_f32_e32 v16, 0xc1000000, v16
	v_mul_f32_e32 v16, v49, v16
	v_mul_f32_e32 v16, 0x3fb8aa3b, v16
	v_exp_f32_e32 v16, v16
	s_nop 0
	v_fma_f32 v18, -v16, v16, 1.0
	v_max_f32_e32 v18, 0, v18
	v_sqrt_f32_e32 v18, v18
	s_nop 0
	v_mul_f32_e32 v17, v17, v18
	ds_write_b32 v46, v16 offset:43648
	v_mul_f32_e32 v17, v154, v17
	v_or_b32_e32 v18, v38, v43
	v_lshl_add_u32 v16, v18, 2, v28
	ds_write_b32 v16, v17
	v_add_f32_e32 v16, v41, v19
	v_mul_f32_e32 v16, 0xbfb8aa3b, v16
	v_exp_f32_e32 v16, v16
	v_add_f32_e32 v17, v40, v23
	v_mul_f32_e32 v17, 0xbfb8aa3b, v17
	v_exp_f32_e32 v17, v17
	v_add_f32_e32 v16, 1.0, v16
	v_rcp_f32_e32 v16, v16
	v_lshlrev_b32_e32 v40, 7, v35
	v_add_f32_e32 v17, 1.0, v17
	v_rcp_f32_e32 v17, v17
	v_mul_f32_e32 v16, 0xc1000000, v16
	v_mul_f32_e32 v16, v49, v16
	v_mul_f32_e32 v16, 0x3fb8aa3b, v16
	v_exp_f32_e32 v16, v16
	v_mov_b32_e32 v41, v105
	v_fma_f32 v18, -v16, v16, 1.0
	v_max_f32_e32 v18, 0, v18
	v_sqrt_f32_e32 v18, v18
	s_nop 0
	v_mul_f32_e32 v17, v17, v18
	ds_write_b32 v44, v16 offset:43648
	v_mul_f32_e32 v17, v155, v17
	v_or_b32_e32 v18, v37, v43
	v_lshl_add_u32 v16, v18, 2, v28
	ds_write_b32 v16, v17
	v_lshl_add_u64 v[16:17], s[2:3], 0, v[40:41]
	v_lshl_add_u64 v[20:21], v[16:17], 0, v[24:25]
	global_load_dwordx4 v[16:19], v[20:21], off
	s_waitcnt vmcnt(0)
	v_mfma_f32_16x16x32_bf16 v[16:19], v[12:15], v[16:19], 0
	global_load_dwordx4 v[20:23], v[20:21], off offset:64
	s_waitcnt vmcnt(0)
	v_mfma_f32_16x16x32_bf16 v[16:19], v[8:11], v[20:23], v[16:19]
	v_lshl_add_u64 v[20:21], s[0:1], 0, v[40:41]
	v_lshl_add_u64 v[24:25], v[20:21], 0, v[24:25]
	global_load_dwordx4 v[20:23], v[24:25], off
	s_waitcnt vmcnt(0)
	v_mfma_f32_16x16x32_bf16 v[12:15], v[12:15], v[20:23], 0
	global_load_dwordx4 v[20:23], v[24:25], off offset:64
	s_waitcnt vmcnt(0)
	v_mfma_f32_16x16x32_bf16 v[8:11], v[8:11], v[20:23], v[12:15]
	s_nop 4
	v_add_f32_e32 v14, v33, v16
	v_mul_f32_e64 v13, |v34|, s14
	v_mul_f32_e32 v14, 0xbfb8aa3b, v14
	v_exp_f32_e32 v13, v13
	v_exp_f32_e32 v14, v14
	v_max_f32_e64 v12, -v34, -v34
	v_max_f32_e32 v12, 0, v12
	v_add_f32_e32 v13, 1.0, v13
	v_add_f32_e32 v14, 1.0, v14
	v_log_f32_e32 v13, v13
	v_rcp_f32_e32 v14, v14
	v_add_f32_e32 v8, v32, v8
	v_mul_f32_e32 v8, 0xbfb8aa3b, v8
	v_fmac_f32_e32 v12, 0x3f317218, v13
	v_mul_f32_e32 v14, 0xc1000000, v14
	v_mul_f32_e32 v14, v12, v14
	v_mul_f32_e32 v14, 0x3fb8aa3b, v14
	v_exp_f32_e32 v14, v14
	v_exp_f32_e32 v8, v8
	v_or_b32_e32 v13, s73, v35
	v_add_f32_e32 v9, v32, v9
	v_fma_f32 v15, -v14, v14, 1.0
	v_add_f32_e32 v8, 1.0, v8
	v_max_f32_e32 v15, 0, v15
	v_rcp_f32_e32 v8, v8
	v_sqrt_f32_e32 v15, v15
	v_mul_f32_e32 v9, 0xbfb8aa3b, v9
	v_exp_f32_e32 v9, v9
	v_mul_f32_e32 v8, v8, v15
	ds_write_b32 v48, v14 offset:43712
	v_add_f32_e32 v9, 1.0, v9
	v_rcp_f32_e32 v9, v9
	v_mul_f32_e32 v8, v156, v8
	v_or_b32_e32 v15, v42, v13
	v_lshl_add_u32 v14, v15, 2, v28
	ds_write_b32 v14, v8
	v_add_f32_e32 v8, v33, v17
	v_mul_f32_e32 v8, 0xbfb8aa3b, v8
	v_exp_f32_e32 v8, v8
	s_nop 0
	v_add_f32_e32 v8, 1.0, v8
	v_rcp_f32_e32 v8, v8
	s_nop 0
	v_mul_f32_e32 v8, 0xc1000000, v8
	v_mul_f32_e32 v8, v12, v8
	v_mul_f32_e32 v8, 0x3fb8aa3b, v8
	v_exp_f32_e32 v8, v8
	s_nop 0
	v_fma_f32 v14, -v8, v8, 1.0
	v_max_f32_e32 v14, 0, v14
	v_sqrt_f32_e32 v14, v14
	s_nop 0
	v_mul_f32_e32 v9, v9, v14
	ds_write_b32 v47, v8 offset:43712
	v_mul_f32_e32 v9, v157, v9
	v_or_b32_e32 v14, v39, v13
	v_lshl_add_u32 v8, v14, 2, v28
	ds_write_b32 v8, v9
	v_add_f32_e32 v8, v33, v18
	v_mul_f32_e32 v8, 0xbfb8aa3b, v8
	v_exp_f32_e32 v8, v8
	v_add_f32_e32 v9, v32, v10
	v_mul_f32_e32 v9, 0xbfb8aa3b, v9
	v_exp_f32_e32 v9, v9
	v_add_f32_e32 v8, 1.0, v8
	v_rcp_f32_e32 v8, v8
	v_add_f32_e32 v9, 1.0, v9
	v_rcp_f32_e32 v9, v9
	v_mul_f32_e32 v8, 0xc1000000, v8
	v_mul_f32_e32 v8, v12, v8
	v_mul_f32_e32 v8, 0x3fb8aa3b, v8
	v_exp_f32_e32 v8, v8
	s_nop 0
	v_fma_f32 v10, -v8, v8, 1.0
	v_max_f32_e32 v10, 0, v10
	v_sqrt_f32_e32 v10, v10
	s_nop 0
	v_mul_f32_e32 v9, v9, v10
	ds_write_b32 v46, v8 offset:43712
	v_mul_f32_e32 v9, v158, v9
	v_or_b32_e32 v10, v38, v13
	v_lshl_add_u32 v8, v10, 2, v28
	ds_write_b32 v8, v9
	v_add_f32_e32 v8, v33, v19
	v_mul_f32_e32 v8, 0xbfb8aa3b, v8
	v_exp_f32_e32 v8, v8
	v_add_f32_e32 v9, v32, v11
	v_mul_f32_e32 v9, 0xbfb8aa3b, v9
	v_exp_f32_e32 v9, v9
	v_add_f32_e32 v8, 1.0, v8
	v_rcp_f32_e32 v8, v8
	v_add_f32_e32 v9, 1.0, v9
	v_rcp_f32_e32 v9, v9
	v_mul_f32_e32 v8, 0xc1000000, v8
	v_mul_f32_e32 v8, v12, v8
	v_mul_f32_e32 v8, 0x3fb8aa3b, v8
	v_exp_f32_e32 v8, v8
	v_ashrrev_i32_e32 v12, 8, v30
	v_fma_f32 v10, -v8, v8, 1.0
	v_max_f32_e32 v10, 0, v10
	v_sqrt_f32_e32 v10, v10
	s_nop 0
	v_mul_f32_e32 v9, v9, v10
	ds_write_b32 v44, v8 offset:43712
	v_mul_f32_e32 v9, v159, v9
	v_or_b32_e32 v10, v37, v13
	v_lshl_add_u32 v8, v10, 2, v28
	ds_write_b32 v8, v9
	v_bfe_u32 v8, v30, 6, 2
	v_lshlrev_b32_e32 v9, 4, v8
	v_xor_b32_e32 v10, 63, v9
	v_cndmask_b32_e32 v25, v10, v9, vcc
	v_lshl_or_b32 v10, v12, 14, v104
	v_lshl_or_b32 v11, v25, 8, v10
	s_waitcnt lgkmcnt(0)
	s_barrier
	v_add_u32_e32 v13, v111, v11
	v_add_u32_e32 v11, v28, v11
	ds_read_b32 v17, v13 offset:43520
	ds_read_b32 v22, v11
	v_or_b32_e32 v11, 1, v9
	v_xor_b32_e32 v177, 62, v9
	v_cndmask_b32_e32 v19, v177, v11, vcc
	v_lshl_or_b32 v11, v19, 8, v10
	v_add_u32_e32 v179, v111, v11
	v_add_u32_e32 v11, v28, v11
	ds_read_b32 v15, v11
	ds_read_b32 v161, v179 offset:43520
	v_or_b32_e32 v11, 2, v9
	v_xor_b32_e32 v176, 61, v9
	v_cndmask_b32_e32 v20, v176, v11, vcc
	v_lshl_or_b32 v11, v20, 8, v10
	v_add_u32_e32 v178, v111, v11
	v_add_u32_e32 v11, v28, v11
	ds_read_b32 v16, v11
	ds_read_b32 v162, v178 offset:43520
	v_or_b32_e32 v11, 3, v9
	v_xor_b32_e32 v177, 60, v9
	v_cndmask_b32_e32 v21, v177, v11, vcc
	v_lshl_or_b32 v11, v21, 8, v10
	v_add_u32_e32 v179, v111, v11
	v_add_u32_e32 v11, v28, v11
	ds_read_b32 v18, v11
	ds_read_b32 v163, v179 offset:43520
	v_or_b32_e32 v11, 4, v9
	v_xor_b32_e32 v176, 59, v9
	v_cndmask_b32_e32 v36, v176, v11, vcc
	v_lshl_or_b32 v11, v36, 8, v10
	v_add_u32_e32 v178, v111, v11
	v_add_u32_e32 v11, v28, v11
	ds_read_b32 v33, v11
	ds_read_b32 v164, v178 offset:43520
	v_or_b32_e32 v11, 5, v9
	v_xor_b32_e32 v177, 58, v9
	v_cndmask_b32_e32 v37, v177, v11, vcc
	v_lshl_or_b32 v11, v37, 8, v10
	v_add_u32_e32 v179, v111, v11
	v_add_u32_e32 v11, v28, v11
	ds_read_b32 v34, v11
	ds_read_b32 v165, v179 offset:43520
	v_or_b32_e32 v11, 6, v9
	v_xor_b32_e32 v176, 57, v9
	v_cndmask_b32_e32 v39, v176, v11, vcc
	v_lshl_or_b32 v11, v39, 8, v10
	v_add_u32_e32 v178, v111, v11
	v_add_u32_e32 v11, v28, v11
	ds_read_b32 v35, v11
	ds_read_b32 v166, v178 offset:43520
	v_or_b32_e32 v11, 7, v9
	v_xor_b32_e32 v177, 56, v9
	v_cndmask_b32_e32 v45, v177, v11, vcc
	v_lshl_or_b32 v11, v45, 8, v10
	v_add_u32_e32 v179, v111, v11
	v_add_u32_e32 v11, v28, v11
	ds_read_b32 v42, v11
	ds_read_b32 v167, v179 offset:43520
	v_or_b32_e32 v11, 8, v9
	v_xor_b32_e32 v176, 55, v9
	v_cndmask_b32_e32 v46, v176, v11, vcc
	v_lshl_or_b32 v11, v46, 8, v10
	v_add_u32_e32 v178, v111, v11
	v_add_u32_e32 v11, v28, v11
	ds_read_b32 v43, v11
	ds_read_b32 v168, v178 offset:43520
	v_or_b32_e32 v11, 9, v9
	v_xor_b32_e32 v177, 54, v9
	v_cndmask_b32_e32 v48, v177, v11, vcc
	v_lshl_or_b32 v11, v48, 8, v10
	v_add_u32_e32 v179, v111, v11
	v_add_u32_e32 v11, v28, v11
	ds_read_b32 v44, v11
	ds_read_b32 v169, v179 offset:43520
	v_or_b32_e32 v11, 10, v9
	v_xor_b32_e32 v176, 53, v9
	v_cndmask_b32_e32 v54, v176, v11, vcc
	v_lshl_or_b32 v11, v54, 8, v10
	v_add_u32_e32 v178, v111, v11
	v_add_u32_e32 v11, v28, v11
	ds_read_b32 v51, v11
	ds_read_b32 v170, v178 offset:43520
	v_or_b32_e32 v11, 11, v9
	v_xor_b32_e32 v177, 52, v9
	v_cndmask_b32_e32 v55, v177, v11, vcc
	v_lshl_or_b32 v11, v55, 8, v10
	v_add_u32_e32 v179, v111, v11
	v_add_u32_e32 v11, v28, v11
	ds_read_b32 v52, v11
	ds_read_b32 v171, v179 offset:43520
	v_or_b32_e32 v11, 12, v9
	v_xor_b32_e32 v176, 51, v9
	v_cndmask_b32_e32 v57, v176, v11, vcc
	v_lshl_or_b32 v11, v57, 8, v10
	v_add_u32_e32 v178, v111, v11
	v_add_u32_e32 v11, v28, v11
	ds_read_b32 v53, v11
	ds_read_b32 v172, v178 offset:43520
	v_or_b32_e32 v11, 13, v9
	v_xor_b32_e32 v177, 50, v9
	v_cndmask_b32_e32 v62, v177, v11, vcc
	v_lshl_or_b32 v11, v62, 8, v10
	v_add_u32_e32 v179, v111, v11
	v_add_u32_e32 v11, v28, v11
	ds_read_b32 v60, v11
	ds_read_b32 v173, v179 offset:43520
	v_or_b32_e32 v11, 14, v9
	v_xor_b32_e32 v176, 49, v9
	v_cndmask_b32_e32 v63, v176, v11, vcc
	v_lshl_or_b32 v11, v63, 8, v10
	v_add_u32_e32 v178, v111, v11
	v_add_u32_e32 v11, v28, v11
	ds_read_b32 v61, v11
	ds_read_b32 v174, v178 offset:43520
	v_or_b32_e32 v11, 15, v9
	v_xor_b32_e32 v177, 48, v9
	v_cndmask_b32_e32 v65, v177, v11, vcc
	v_lshl_or_b32 v11, v65, 8, v10
	v_add_u32_e32 v179, v111, v11
	v_add_u32_e32 v11, v28, v11
	ds_read_b32 v32, v11
	ds_read_b32 v175, v179 offset:43520
	v_and_b32_e32 v9, 0x3fffff00, v30
	v_lshlrev_b32_e32 v10, 6, v8
	v_cmp_ne_u32_e32 vcc, 0, v8
	v_or3_b32 v9, v10, v9, v31
	s_waitcnt lgkmcnt(0)
	v_fmac_f32_e32 v22, 0, v17
	v_fmac_f32_e32 v15, v22, v161
	v_mul_f32_e32 v13, v17, v161
	v_fmac_f32_e32 v16, v15, v162
	v_mul_f32_e32 v14, v13, v162
	v_fmac_f32_e32 v18, v16, v163
	v_mul_f32_e32 v38, v14, v163
	v_fmac_f32_e32 v33, v18, v164
	v_mul_f32_e32 v23, v38, v164
	v_fmac_f32_e32 v34, v33, v165
	v_mul_f32_e32 v24, v23, v165
	v_fmac_f32_e32 v35, v34, v166
	v_mul_f32_e32 v47, v24, v166
	v_fmac_f32_e32 v42, v35, v167
	v_mul_f32_e32 v40, v47, v167
	v_fmac_f32_e32 v43, v42, v168
	v_mul_f32_e32 v41, v40, v168
	v_fmac_f32_e32 v44, v43, v169
	v_mul_f32_e32 v56, v41, v169
	v_fmac_f32_e32 v51, v44, v170
	v_mul_f32_e32 v49, v56, v170
	v_fmac_f32_e32 v52, v51, v171
	v_mul_f32_e32 v50, v49, v171
	v_fmac_f32_e32 v53, v52, v172
	v_mul_f32_e32 v64, v50, v172
	v_fmac_f32_e32 v60, v53, v173
	v_mul_f32_e32 v58, v64, v173
	v_fmac_f32_e32 v61, v60, v174
	v_mul_f32_e32 v59, v58, v174
	v_fmac_f32_e32 v32, v61, v175
	v_mul_f32_e32 v66, v59, v175
	v_lshlrev_b32_e32 v9, 2, v9
	v_add_u32_e32 v10, v27, v9
	v_add_u32_e32 v9, v29, v9
	ds_write_b32 v10, v66
	ds_write_b32 v9, v32
	s_waitcnt lgkmcnt(0)
	s_barrier
	v_and_b32_e32 v9, 0x3fffff3f, v30
	v_lshlrev_b32_e32 v10, 2, v9
	v_add_u32_e32 v11, v27, v10
	v_add_u32_e32 v10, v29, v10
	ds_read_b32 v216, v11
	ds_read_b32 v217, v10
	ds_read_b32 v218, v11 offset:256
	ds_read_b32 v219, v10 offset:256
	ds_read_b32 v220, v11 offset:512
	ds_read_b32 v221, v10 offset:512
	v_readfirstlane_b32 s0, v8
	v_cmp_eq_u32_e32 vcc, 3, v8
	s_waitcnt lgkmcnt(0)
	s_cmp_eq_u32 s0, 0
	s_cbranch_scc1 .Llru_cdone
	v_mov_b32_e32 v67, v216
	v_mov_b32_e32 v68, v217
	s_cmp_lt_u32 s0, 2
	s_cbranch_scc1 .Llru_cdone
	v_fma_f32 v68, v68, v218, v219
	v_mul_f32_e32 v67, v67, v218
	s_cmp_lg_u32 s0, 3
	s_cbranch_scc1 .Llru_cdone
	v_fma_f32 v68, v68, v220, v221
	v_mul_f32_e32 v67, v67, v220
.Llru_cdone:
	s_add_i32 s17, s17, s36
	v_or_b32_e32 v30, s17, v25
	v_or_b32_e32 v104, s28, v31
	v_ashrrev_i32_e32 v31, 31, v30
	v_lshlrev_b64 v[30:31], 10, v[30:31]
	v_mov_b64_e32 v[8:9], s[8:9]
	v_lshl_add_u64 v[30:31], v[30:31], 0, v[104:105]
	v_fmac_f32_e32 v22, v17, v68
	v_mad_i64_i32 v[10:11], s[0:1], v12, s42, v[8:9]
	v_bfe_u32 v25, v22, 16, 1
	v_lshlrev_b64 v[30:31], 1, v[30:31]
	v_mov_b64_e32 v[8:9], s[10:11]
	v_add3_u32 v22, v22, v25, s25
	v_lshl_add_u64 v[70:71], v[10:11], 0, v[30:31]
	v_mul_f32_e32 v17, v17, v67
	v_mad_i64_i32 v[8:9], s[0:1], v12, s42, v[8:9]
	global_store_short_d16_hi v[70:71], v22, off
	v_bfe_u32 v22, v17, 16, 1
	v_add3_u32 v17, v17, v22, s25
	v_lshl_add_u64 v[30:31], v[8:9], 0, v[30:31]
	global_store_short_d16_hi v[30:31], v17, off
	v_or_b32_e32 v30, s17, v19
	v_ashrrev_i32_e32 v31, 31, v30
	v_lshlrev_b64 v[30:31], 10, v[30:31]
	v_lshl_add_u64 v[30:31], v[30:31], 0, v[104:105]
	v_fmac_f32_e32 v15, v13, v68
	v_bfe_u32 v17, v15, 16, 1
	v_lshlrev_b64 v[30:31], 1, v[30:31]
	v_add3_u32 v15, v15, v17, s25
	v_lshl_add_u64 v[70:71], v[10:11], 0, v[30:31]
	v_mul_f32_e32 v13, v13, v67
	global_store_short_d16_hi v[70:71], v15, off
	v_bfe_u32 v15, v13, 16, 1
	v_add3_u32 v13, v13, v15, s25
	v_lshl_add_u64 v[30:31], v[8:9], 0, v[30:31]
	global_store_short_d16_hi v[30:31], v13, off
	v_or_b32_e32 v30, s17, v20
	v_ashrrev_i32_e32 v31, 31, v30
	v_lshlrev_b64 v[30:31], 10, v[30:31]
	v_fmac_f32_e32 v16, v14, v68
	v_lshl_add_u64 v[30:31], v[30:31], 0, v[104:105]
	v_bfe_u32 v13, v16, 16, 1
	v_add3_u32 v13, v16, v13, s25
	v_lshlrev_b64 v[16:17], 1, v[30:31]
	v_lshl_add_u64 v[30:31], v[10:11], 0, v[16:17]
	global_store_short_d16_hi v[30:31], v13, off
	v_mul_f32_e32 v13, v14, v67
	v_bfe_u32 v14, v13, 16, 1
	v_add3_u32 v13, v13, v14, s25
	v_lshl_add_u64 v[14:15], v[8:9], 0, v[16:17]
	global_store_short_d16_hi v[14:15], v13, off
	v_or_b32_e32 v14, s17, v21
	v_ashrrev_i32_e32 v15, 31, v14
	v_lshlrev_b64 v[14:15], 10, v[14:15]
	v_lshl_add_u64 v[14:15], v[14:15], 0, v[104:105]
	v_fmac_f32_e32 v18, v38, v68
	v_bfe_u32 v13, v18, 16, 1
	v_lshlrev_b64 v[14:15], 1, v[14:15]
	v_add3_u32 v13, v18, v13, s25
	v_lshl_add_u64 v[16:17], v[10:11], 0, v[14:15]
	global_store_short_d16_hi v[16:17], v13, off
	v_mul_f32_e32 v13, v38, v67
	v_bfe_u32 v16, v13, 16, 1
	v_add3_u32 v13, v13, v16, s25
	v_lshl_add_u64 v[14:15], v[8:9], 0, v[14:15]
	global_store_short_d16_hi v[14:15], v13, off
	v_or_b32_e32 v14, s17, v36
	v_ashrrev_i32_e32 v15, 31, v14
	v_lshlrev_b64 v[14:15], 10, v[14:15]
	v_lshl_add_u64 v[14:15], v[14:15], 0, v[104:105]
	v_fmac_f32_e32 v33, v23, v68
	v_bfe_u32 v13, v33, 16, 1
	v_lshlrev_b64 v[14:15], 1, v[14:15]
	v_add3_u32 v13, v33, v13, s25
	v_lshl_add_u64 v[16:17], v[10:11], 0, v[14:15]
	global_store_short_d16_hi v[16:17], v13, off
	v_mul_f32_e32 v13, v23, v67
	v_bfe_u32 v16, v13, 16, 1
	v_add3_u32 v13, v13, v16, s25
	v_lshl_add_u64 v[14:15], v[8:9], 0, v[14:15]
	global_store_short_d16_hi v[14:15], v13, off
	v_or_b32_e32 v14, s17, v37
	v_ashrrev_i32_e32 v15, 31, v14
	v_lshlrev_b64 v[14:15], 10, v[14:15]
	v_lshl_add_u64 v[14:15], v[14:15], 0, v[104:105]
	v_fmac_f32_e32 v34, v24, v68
	v_bfe_u32 v13, v34, 16, 1
	v_lshlrev_b64 v[14:15], 1, v[14:15]
	v_add3_u32 v13, v34, v13, s25
	v_lshl_add_u64 v[16:17], v[10:11], 0, v[14:15]
	global_store_short_d16_hi v[16:17], v13, off
	v_mul_f32_e32 v13, v24, v67
	v_bfe_u32 v16, v13, 16, 1
	v_add3_u32 v13, v13, v16, s25
	v_lshl_add_u64 v[14:15], v[8:9], 0, v[14:15]
	global_store_short_d16_hi v[14:15], v13, off
	v_or_b32_e32 v14, s17, v39
	v_ashrrev_i32_e32 v15, 31, v14
	v_lshlrev_b64 v[14:15], 10, v[14:15]
	v_lshl_add_u64 v[14:15], v[14:15], 0, v[104:105]
	v_fmac_f32_e32 v35, v47, v68
	v_bfe_u32 v13, v35, 16, 1
	v_lshlrev_b64 v[14:15], 1, v[14:15]
	v_add3_u32 v13, v35, v13, s25
	v_lshl_add_u64 v[16:17], v[10:11], 0, v[14:15]
	global_store_short_d16_hi v[16:17], v13, off
	v_mul_f32_e32 v13, v47, v67
	v_bfe_u32 v16, v13, 16, 1
	v_add3_u32 v13, v13, v16, s25
	v_lshl_add_u64 v[14:15], v[8:9], 0, v[14:15]
	global_store_short_d16_hi v[14:15], v13, off
	v_or_b32_e32 v14, s17, v45
	v_ashrrev_i32_e32 v15, 31, v14
	v_lshlrev_b64 v[14:15], 10, v[14:15]
	v_lshl_add_u64 v[14:15], v[14:15], 0, v[104:105]
	v_fmac_f32_e32 v42, v40, v68
	v_bfe_u32 v13, v42, 16, 1
	v_lshlrev_b64 v[14:15], 1, v[14:15]
	v_add3_u32 v13, v42, v13, s25
	v_lshl_add_u64 v[16:17], v[10:11], 0, v[14:15]
	global_store_short_d16_hi v[16:17], v13, off
	v_mul_f32_e32 v13, v40, v67
	v_bfe_u32 v16, v13, 16, 1
	v_add3_u32 v13, v13, v16, s25
	v_lshl_add_u64 v[14:15], v[8:9], 0, v[14:15]
	global_store_short_d16_hi v[14:15], v13, off
	v_or_b32_e32 v14, s17, v46
	v_ashrrev_i32_e32 v15, 31, v14
	v_lshlrev_b64 v[14:15], 10, v[14:15]
	v_lshl_add_u64 v[14:15], v[14:15], 0, v[104:105]
	v_fmac_f32_e32 v43, v41, v68
	v_bfe_u32 v13, v43, 16, 1
	v_lshlrev_b64 v[14:15], 1, v[14:15]
	v_add3_u32 v13, v43, v13, s25
	v_lshl_add_u64 v[16:17], v[10:11], 0, v[14:15]
	global_store_short_d16_hi v[16:17], v13, off
	v_mul_f32_e32 v13, v41, v67
	v_bfe_u32 v16, v13, 16, 1
	v_add3_u32 v13, v13, v16, s25
	v_lshl_add_u64 v[14:15], v[8:9], 0, v[14:15]
	global_store_short_d16_hi v[14:15], v13, off
	v_or_b32_e32 v14, s17, v48
	v_ashrrev_i32_e32 v15, 31, v14
	v_lshlrev_b64 v[14:15], 10, v[14:15]
	v_lshl_add_u64 v[14:15], v[14:15], 0, v[104:105]
	v_fmac_f32_e32 v44, v56, v68
	v_bfe_u32 v13, v44, 16, 1
	v_lshlrev_b64 v[14:15], 1, v[14:15]
	v_add3_u32 v13, v44, v13, s25
	v_lshl_add_u64 v[16:17], v[10:11], 0, v[14:15]
	global_store_short_d16_hi v[16:17], v13, off
	v_mul_f32_e32 v13, v56, v67
	v_bfe_u32 v16, v13, 16, 1
	v_add3_u32 v13, v13, v16, s25
	v_lshl_add_u64 v[14:15], v[8:9], 0, v[14:15]
	global_store_short_d16_hi v[14:15], v13, off
	v_or_b32_e32 v14, s17, v54
	v_ashrrev_i32_e32 v15, 31, v14
	v_lshlrev_b64 v[14:15], 10, v[14:15]
	v_lshl_add_u64 v[14:15], v[14:15], 0, v[104:105]
	v_fmac_f32_e32 v51, v49, v68
	v_bfe_u32 v13, v51, 16, 1
	v_lshlrev_b64 v[14:15], 1, v[14:15]
	v_add3_u32 v13, v51, v13, s25
	v_lshl_add_u64 v[16:17], v[10:11], 0, v[14:15]
	global_store_short_d16_hi v[16:17], v13, off
	v_mul_f32_e32 v13, v49, v67
	v_bfe_u32 v16, v13, 16, 1
	v_add3_u32 v13, v13, v16, s25
	v_lshl_add_u64 v[14:15], v[8:9], 0, v[14:15]
	global_store_short_d16_hi v[14:15], v13, off
	v_or_b32_e32 v14, s17, v55
	v_ashrrev_i32_e32 v15, 31, v14
	v_lshlrev_b64 v[14:15], 10, v[14:15]
	v_lshl_add_u64 v[14:15], v[14:15], 0, v[104:105]
	v_fmac_f32_e32 v52, v50, v68
	v_bfe_u32 v13, v52, 16, 1
	v_lshlrev_b64 v[14:15], 1, v[14:15]
	v_add3_u32 v13, v52, v13, s25
	v_lshl_add_u64 v[16:17], v[10:11], 0, v[14:15]
	global_store_short_d16_hi v[16:17], v13, off
	v_mul_f32_e32 v13, v50, v67
	v_bfe_u32 v16, v13, 16, 1
	v_add3_u32 v13, v13, v16, s25
	v_lshl_add_u64 v[14:15], v[8:9], 0, v[14:15]
	global_store_short_d16_hi v[14:15], v13, off
	v_or_b32_e32 v14, s17, v57
	v_ashrrev_i32_e32 v15, 31, v14
	v_lshlrev_b64 v[14:15], 10, v[14:15]
	v_lshl_add_u64 v[14:15], v[14:15], 0, v[104:105]
	v_fmac_f32_e32 v53, v64, v68
	v_bfe_u32 v13, v53, 16, 1
	v_lshlrev_b64 v[14:15], 1, v[14:15]
	v_add3_u32 v13, v53, v13, s25
	v_lshl_add_u64 v[16:17], v[10:11], 0, v[14:15]
	global_store_short_d16_hi v[16:17], v13, off
	v_mul_f32_e32 v13, v64, v67
	v_bfe_u32 v16, v13, 16, 1
	v_add3_u32 v13, v13, v16, s25
	v_lshl_add_u64 v[14:15], v[8:9], 0, v[14:15]
	global_store_short_d16_hi v[14:15], v13, off
	v_or_b32_e32 v14, s17, v62
	v_ashrrev_i32_e32 v15, 31, v14
	v_lshlrev_b64 v[14:15], 10, v[14:15]
	v_lshl_add_u64 v[14:15], v[14:15], 0, v[104:105]
	v_fmac_f32_e32 v60, v58, v68
	v_bfe_u32 v13, v60, 16, 1
	v_lshlrev_b64 v[14:15], 1, v[14:15]
	v_add3_u32 v13, v60, v13, s25
	v_lshl_add_u64 v[16:17], v[10:11], 0, v[14:15]
	global_store_short_d16_hi v[16:17], v13, off
	v_mul_f32_e32 v13, v58, v67
	v_bfe_u32 v16, v13, 16, 1
	v_add3_u32 v13, v13, v16, s25
	v_lshl_add_u64 v[14:15], v[8:9], 0, v[14:15]
	global_store_short_d16_hi v[14:15], v13, off
	v_or_b32_e32 v14, s17, v63
	v_ashrrev_i32_e32 v15, 31, v14
	v_lshlrev_b64 v[14:15], 10, v[14:15]
	v_lshl_add_u64 v[14:15], v[14:15], 0, v[104:105]
	v_fmac_f32_e32 v61, v59, v68
	v_bfe_u32 v13, v61, 16, 1
	v_lshlrev_b64 v[14:15], 1, v[14:15]
	v_add3_u32 v13, v61, v13, s25
	v_lshl_add_u64 v[16:17], v[10:11], 0, v[14:15]
	global_store_short_d16_hi v[16:17], v13, off
	v_mul_f32_e32 v13, v59, v67
	v_bfe_u32 v16, v13, 16, 1
	v_add3_u32 v13, v13, v16, s25
	v_lshl_add_u64 v[14:15], v[8:9], 0, v[14:15]
	global_store_short_d16_hi v[14:15], v13, off
	v_or_b32_e32 v14, s17, v65
	v_ashrrev_i32_e32 v15, 31, v14
	v_lshlrev_b64 v[14:15], 10, v[14:15]
	v_lshl_add_u64 v[14:15], v[14:15], 0, v[104:105]
	v_fmac_f32_e32 v32, v66, v68
	v_bfe_u32 v13, v32, 16, 1
	v_lshlrev_b64 v[14:15], 1, v[14:15]
	v_add3_u32 v13, v32, v13, s25
	v_lshl_add_u64 v[10:11], v[10:11], 0, v[14:15]
	global_store_short_d16_hi v[10:11], v13, off
	v_mul_f32_e32 v10, v66, v67
	v_bfe_u32 v11, v10, 16, 1
	v_add3_u32 v11, v10, v11, s25
	v_lshl_add_u64 v[8:9], v[8:9], 0, v[14:15]
	global_store_short_d16_hi v[8:9], v11, off
	s_and_saveexec_b64 s[0:1], vcc
	s_cbranch_execz .LBB0_359
	v_mul_hi_i32_i24_e32 v9, 0x88, v12
	v_mul_i32_i24_e32 v8, 0x88, v12
	s_ashr_i32 s17, s16, 31
	v_lshl_add_u64 v[8:9], v[8:9], 0, s[16:17]
	v_lshlrev_b64 v[8:9], 12, v[8:9]
	v_lshl_add_u64 v[8:9], s[12:13], 0, v[8:9]
	v_lshlrev_b64 v[14:15], 2, v[104:105]
	v_lshl_add_u64 v[8:9], v[8:9], 0, v[14:15]
	global_store_dword v[8:9], v10, off
	v_add_u32_e32 v10, 2, v12
	v_mov_b64_e32 v[8:9], s[16:17]
	s_movk_i32 s2, 0x88
	v_mad_i64_i32 v[8:9], s[2:3], v10, s2, v[8:9]
	v_lshlrev_b64 v[8:9], 12, v[8:9]
	v_lshl_add_u64 v[8:9], s[12:13], 0, v[8:9]
	v_lshl_add_u64 v[8:9], v[8:9], 0, v[14:15]
	global_store_dword v[8:9], v32, off
	s_branch .LBB0_359
